# speedup vs baseline: 1.0138x; 1.0036x over previous
.LBB3_4:
	s_lshl_b32 s18, s24, 8
	s_and_b32 s18, s18, 0x300
	s_lshl_b64 s[0:1], s[0:1], 10
	s_or_b32 s0, s0, s18
	s_lshl_b32 s18, s33, 5
	s_add_u32 s18, s0, s18
	v_and_b32_e32 v203, 31, v0
	s_addc_u32 s19, s1, 0
	v_or_b32_e32 v2, s18, v203
	v_mov_b32_e32 v3, s19
	v_lshrrev_b32_e32 v204, 5, v1
	v_lshlrev_b64 v[4:5], 10, v[2:3]
	v_lshlrev_b64 v[2:3], 12, v[2:3]
	v_lshl_add_u64 v[2:3], s[14:15], 0, v[2:3]
	v_lshlrev_b32_e32 v28, 4, v204
	v_mov_b32_e32 v29, 0
	v_lshl_add_u64 v[26:27], v[2:3], 0, v[28:29]
	v_lshl_add_u64 v[2:3], s[8:9], 0, v[4:5]
	v_lshl_add_u64 v[2:3], v[2:3], 0, s[6:7]
	v_and_b32_e32 v28, 32, v0
	v_lshl_add_u64 v[40:41], v[2:3], 0, v[28:29]
	global_load_dwordx4 v[100:103], v[40:41], off offset:16
	global_load_dwordx4 v[96:99], v[40:41], off
	v_mul_hi_u32_u24_e32 v21, 0x1800, v20
	s_and_b64 vcc, exec, s[4:5]
	v_mul_u32_u24_e32 v20, 0x1800, v20
	s_cbranch_vccnz .LBB3_6
	s_mov_b64 s[0:1], 0x20000
	s_cmp_lg_u32 0, -1
	v_lshl_add_u64 v[26:27], v[22:23], 0, s[0:1]
	s_cselect_b32 s0, 0, 0
	s_add_i32 s0, s0, s35
	s_addk_i32 s0, 0x4000
	s_mov_b32 m0, s0
	s_nop 0
	global_load_lds_dwordx4 v[26:27], off
.LBB3_6:
	v_lshlrev_b32_e32 v104, 3, v24
	v_or_b32_e32 v24, s18, v30
	v_mov_b32_e32 v25, s19
	v_lshlrev_b64 v[24:25], 12, v[24:25]
	v_lshl_add_u64 v[80:81], s[14:15], 0, v[24:25]
	v_lshrrev_b32_e32 v106, 2, v203
	v_lshlrev_b32_e32 v24, 1, v204
	v_bfe_u32 v25, v203, 2, 2
	s_lshl_b32 s7, s33, 13
	v_bitop3_b32 v26, v24, v106, 3 bitop3:0x78
	v_bitop3_b32 v24, v24, v25, 1 bitop3:0x36
	s_cmp_lg_u32 0, -1
	v_lshlrev_b32_e32 v218, 4, v24
	v_bitop3_b32 v24, v30, v0, 15 bitop3:0x78
	s_cselect_b32 s0, 0, 0
	v_lshlrev_b32_e32 v28, 4, v24
	s_add_i32 s23, s0, s7
	v_lshl_add_u64 v[164:165], v[80:81], 0, v[28:29]
	s_mov_b64 s[0:1], 0x0
	v_and_b32_e32 v105, 15, v0
	v_lshl_add_u64 v[24:25], v[164:165], 0, s[0:1]
	s_add_i32 s36, s23, 0x14800
	s_mov_b32 m0, s36
	s_nop 0
	global_load_lds_dwordx4 v[24:25], off nt
	v_bitop3_b32 v24, v30, v105, 4 bitop3:0x36
	v_lshlrev_b32_e32 v28, 4, v24
	v_lshl_add_u64 v[24:25], v[80:81], 0, v[28:29]
	s_mov_b64 s[8:9], 0x4000
	v_lshlrev_b32_e32 v217, 4, v26
	v_lshl_add_u64 v[26:27], v[24:25], 0, s[8:9]
	s_add_i32 s8, s23, 0x14c00
	s_mov_b32 m0, s8
	s_nop 0
	global_load_lds_dwordx4 v[26:27], off nt
	v_bitop3_b32 v26, v30, v105, 8 bitop3:0x36
	v_lshlrev_b32_e32 v28, 4, v26
	v_lshl_add_u64 v[26:27], v[80:81], 0, v[28:29]
	s_mov_b64 s[14:15], 0x8000
	v_bitop3_b32 v28, v30, v105, 12 bitop3:0x36
	v_lshl_add_u64 v[82:83], v[26:27], 0, s[14:15]
	s_add_i32 s14, s23, 0x15000
	s_mov_b32 m0, s14
	s_nop 0
	global_load_lds_dwordx4 v[82:83], off nt
	v_lshlrev_b32_e32 v28, 4, v28
	v_lshl_add_u64 v[28:29], v[80:81], 0, v[28:29]
	s_mov_b64 s[14:15], 0xc000
	v_lshl_add_u64 v[80:81], v[28:29], 0, s[14:15]
	s_add_i32 s14, s23, 0x15400
	s_mov_b32 m0, s14
	s_nop 0
	global_load_lds_dwordx4 v[80:81], off nt
	s_mov_b64 s[26:27], 0x10000
	v_lshl_add_u64 v[80:81], v[164:165], 0, s[26:27]
	s_add_i32 s26, s23, 0x15800
	s_mov_b32 m0, s26
	s_nop 0
	global_load_lds_dwordx4 v[80:81], off nt
	s_mov_b64 s[28:29], 0x14000
	v_lshl_add_u64 v[80:81], v[24:25], 0, s[28:29]
	s_add_i32 s28, s23, 0x15c00
	s_mov_b32 m0, s28
	s_nop 0
	global_load_lds_dwordx4 v[80:81], off nt
	s_mov_b64 s[30:31], 0x18000
	v_lshl_add_u64 v[80:81], v[26:27], 0, s[30:31]
	s_add_i32 s30, s23, 0x16000
	s_mov_b32 m0, s30
	s_nop 0
	global_load_lds_dwordx4 v[80:81], off nt
	s_mov_b64 s[30:31], 0x1c000
	v_lshl_add_u32 v216, v203, 6, 0
	v_lshl_add_u64 v[80:81], v[28:29], 0, s[30:31]
	s_add_i32 s23, s23, 0x16400
	s_mov_b32 m0, s23
	s_nop 0
	global_load_lds_dwordx4 v[80:81], off nt
	s_waitcnt vmcnt(0) lgkmcnt(0)
	s_barrier
	v_and_b32_e32 v226, 31, v0
	v_bfe_u32 v227, v0, 5, 1
	v_lshrrev_b32_e32 v228, 2, v226
	v_lshlrev_b32_e32 v228, 10, v228
	v_and_b32_e32 v229, 3, v226
	v_lshlrev_b32_e32 v229, 8, v229
	v_add3_u32 v230, s36, v228, v229
	v_and_b32_e32 v231, 15, v226
	v_xor_b32_e32 v231, v231, v227
	v_lshlrev_b32_e32 v231, 4, v231
	v_mov_b32_e32 v232, v231
	v_add_u32_e32 v232, v230, v232
	ds_read_b128 v[64:67], v232
	v_xor_b32_e32 v233, 0x80, v231
	v_add_u32_e32 v233, v230, v233
	ds_read_b128 v[2:5], v233
	v_xor_b32_e32 v234, 0x20, v231
	v_add_u32_e32 v234, v230, v234
	ds_read_b128 v[68:71], v234
	v_xor_b32_e32 v235, 0xa0, v231
	v_add_u32_e32 v235, v230, v235
	ds_read_b128 v[6:9], v235
	v_xor_b32_e32 v236, 0x40, v231
	v_add_u32_e32 v236, v230, v236
	ds_read_b128 v[72:75], v236
	v_xor_b32_e32 v237, 0xc0, v231
	v_add_u32_e32 v237, v230, v237
	ds_read_b128 v[10:13], v237
	v_xor_b32_e32 v238, 0x60, v231
	v_add_u32_e32 v238, v230, v238
	ds_read_b128 v[76:79], v238
	v_xor_b32_e32 v239, 0xe0, v231
	v_add_u32_e32 v239, v230, v239
	ds_read_b128 v[14:17], v239
	s_waitcnt lgkmcnt(0)
	s_mov_b64 s[52:53], 0x100
	v_lshl_add_u64 v[224:225], v[164:165], 0, s[52:53]
	s_add_i32 s54, s36, 0x0
	s_mov_b32 m0, s54
	s_nop 0
	global_load_lds_dwordx4 v[224:225], off nt
	s_mov_b64 s[52:53], 0x4100
	v_lshl_add_u64 v[224:225], v[24:25], 0, s[52:53]
	s_add_i32 s54, s36, 0x400
	s_mov_b32 m0, s54
	s_nop 0
	global_load_lds_dwordx4 v[224:225], off nt
	s_mov_b64 s[52:53], 0x8100
	v_lshl_add_u64 v[224:225], v[26:27], 0, s[52:53]
	s_add_i32 s54, s36, 0x800
	s_mov_b32 m0, s54
	s_nop 0
	global_load_lds_dwordx4 v[224:225], off nt
	s_mov_b64 s[52:53], 0xc100
	v_lshl_add_u64 v[224:225], v[28:29], 0, s[52:53]
	s_add_i32 s54, s36, 0xc00
	s_mov_b32 m0, s54
	s_nop 0
	global_load_lds_dwordx4 v[224:225], off nt
	s_mov_b64 s[52:53], 0x10100
	v_lshl_add_u64 v[224:225], v[164:165], 0, s[52:53]
	s_add_i32 s54, s36, 0x1000
	s_mov_b32 m0, s54
	s_nop 0
	global_load_lds_dwordx4 v[224:225], off nt
	s_mov_b64 s[52:53], 0x14100
	v_lshl_add_u64 v[224:225], v[24:25], 0, s[52:53]
	s_add_i32 s54, s36, 0x1400
	s_mov_b32 m0, s54
	s_nop 0
	global_load_lds_dwordx4 v[224:225], off nt
	s_mov_b64 s[52:53], 0x18100
	v_lshl_add_u64 v[224:225], v[26:27], 0, s[52:53]
	s_add_i32 s54, s36, 0x1800
	s_mov_b32 m0, s54
	s_nop 0
	global_load_lds_dwordx4 v[224:225], off nt
	s_mov_b64 s[52:53], 0x1c100
	v_lshl_add_u64 v[224:225], v[28:29], 0, s[52:53]
	s_add_i32 s54, s36, 0x1c00
	s_mov_b32 m0, s54
	s_nop 0
	global_load_lds_dwordx4 v[224:225], off nt
	v_add_u32_e32 v209, v216, v217
	v_add_u32_e32 v210, v216, v218
	ds_read_b128 v[80:83], v209
	ds_read_b128 v[88:91], v209 offset:2048
	ds_read_b128 v[84:87], v210
	ds_read_b128 v[92:95], v210 offset:2048
	v_mov_b32_e32 v219, 0x7f7f7f7f
	v_mov_b32_e32 v220, 0x7c7c7c7c
	s_waitcnt vmcnt(10) lgkmcnt(1)
	v_mfma_scale_f32_32x32x64_f8f6f4 v[64:79], v[80:87], v[96:103], v[64:79], v219, v220 op_sel_hi:[0,0,0]
	s_waitcnt vmcnt(8) lgkmcnt(0)
	v_mfma_scale_f32_32x32x64_f8f6f4 v[2:17], v[88:95], v[96:103], v[2:17], v219, v220 op_sel_hi:[0,0,0]
	s_mov_b32 s39, 0x3fb8aa3b
	s_nop 15
	s_nop 15
	s_nop 15
	s_nop 15
	s_nop 15
	s_nop 15
	s_waitcnt vmcnt(0) lgkmcnt(0)
	s_barrier
	v_lshlrev_b32_e32 v31, 2, v204
	v_max_f32_e32 v80, v65, v65
	v_max_f32_e32 v81, v64, v64
	v_max_f32_e32 v80, v81, v80
	v_max3_f32 v81, v66, v67, v3
	v_max3_f32 v80, v80, v2, v4
	v_max3_f32 v80, v80, v5, v68
	v_max3_f32 v81, v81, v70, v71
	v_max3_f32 v80, v80, v69, v6
	v_max3_f32 v81, v81, v8, v9
	v_max3_f32 v80, v80, v7, v72
	v_max3_f32 v81, v81, v74, v75
	v_max3_f32 v80, v80, v73, v10
	v_max3_f32 v81, v81, v12, v13
	v_max3_f32 v80, v80, v11, v76
	v_max3_f32 v81, v81, v78, v79
	v_max3_f32 v80, v80, v77, v14
	v_max3_f32 v81, v81, v16, v17
	v_max3_f32 v80, v80, v15, v81
	v_mov_b32_e32 v81, v80
	s_nop 1
	v_permlane32_swap_b32_e32 v80, v81
	v_max_f32_e32 v81, v81, v81
	v_max_f32_e32 v80, v80, v80
	v_max_f32_e32 v80, v80, v81
	v_mul_f32_e32 v208, 0x3fb8aa3b, v80
	s_mov_b32 s48, 0
	s_mov_b32 s38, -1
	s_mov_b64 s[0:1], 0x4000
	s_mov_b64 s[8:9], 0x8000
	s_mov_b64 s[24:25], 0xc000
	s_mov_b64 s[14:15], 0x10000
	s_mov_b64 s[26:27], 0x14000
	s_mov_b64 s[28:29], 0x18000
	s_mov_b64 s[30:31], 0x1c000
	v_fma_f32 v64, v64, s39, -v208
	v_fma_f32 v2, v2, s39, -v208
	v_fma_f32 v65, v65, s39, -v208
	v_fma_f32 v3, v3, s39, -v208
	v_fma_f32 v66, v66, s39, -v208
	v_fma_f32 v4, v4, s39, -v208
	v_fma_f32 v67, v67, s39, -v208
	v_fma_f32 v5, v5, s39, -v208
	v_fma_f32 v68, v68, s39, -v208
	v_fma_f32 v6, v6, s39, -v208
	v_fma_f32 v69, v69, s39, -v208
	v_fma_f32 v7, v7, s39, -v208
	v_fma_f32 v70, v70, s39, -v208
	v_fma_f32 v8, v8, s39, -v208
	v_fma_f32 v71, v71, s39, -v208
	v_fma_f32 v9, v9, s39, -v208
	v_fma_f32 v72, v72, s39, -v208
	v_fma_f32 v10, v10, s39, -v208
	v_fma_f32 v73, v73, s39, -v208
	v_fma_f32 v11, v11, s39, -v208
	v_fma_f32 v74, v74, s39, -v208
	v_fma_f32 v12, v12, s39, -v208
	v_fma_f32 v75, v75, s39, -v208
	v_fma_f32 v13, v13, s39, -v208
	v_fma_f32 v76, v76, s39, -v208
	v_fma_f32 v14, v14, s39, -v208
	v_fma_f32 v77, v77, s39, -v208
	v_fma_f32 v78, v78, s39, -v208
	v_fma_f32 v79, v79, s39, -v208
	v_fma_f32 v94, v15, s39, -v208
	v_fma_f32 v16, v16, s39, -v208
	v_fma_f32 v15, v17, s39, -v208
	s_and_b64 vcc, exec, s[4:5]
	s_cbranch_vccnz .LBB3_8
	s_mov_b64 s[42:43], 0x30000
	v_lshl_add_u64 v[22:23], v[22:23], 0, s[42:43]
	s_mov_b32 m0, s37
	s_nop 0
	global_load_lds_dwordx4 v[22:23], off

	.amdhsa_kernel _Z6k_attnILi1024ELi1024ELi1024ELi1024ELi3072ELi1024ELb1ELb1EEvPKDF16_S1_S1_PKfPDF16_
		.amdhsa_group_segment_fixed_size 0
		.amdhsa_private_segment_fixed_size 0
		.amdhsa_kernarg_size 40
		.amdhsa_user_sgpr_count 2
		.amdhsa_user_sgpr_dispatch_ptr 0
		.amdhsa_user_sgpr_queue_ptr 0
		.amdhsa_user_sgpr_kernarg_segment_ptr 1
		.amdhsa_user_sgpr_dispatch_id 0
		.amdhsa_user_sgpr_kernarg_preload_length 0
		.amdhsa_user_sgpr_kernarg_preload_offset 0
		.amdhsa_user_sgpr_private_segment_size 0
		.amdhsa_uses_dynamic_stack 0
		.amdhsa_enable_private_segment 0
		.amdhsa_system_sgpr_workgroup_id_x 1
		.amdhsa_system_sgpr_workgroup_id_y 0
		.amdhsa_system_sgpr_workgroup_id_z 0
		.amdhsa_system_sgpr_workgroup_info 0
		.amdhsa_system_vgpr_workitem_id 0
		.amdhsa_next_free_vgpr 240
		.amdhsa_next_free_sgpr 56
		.amdhsa_accum_offset 240
		.amdhsa_reserve_vcc 1
		.amdhsa_float_round_mode_32 0
		.amdhsa_float_round_mode_16_64 0
		.amdhsa_float_denorm_mode_32 3
		.amdhsa_float_denorm_mode_16_64 3
		.amdhsa_dx10_clamp 1
		.amdhsa_ieee_mode 1
		.amdhsa_fp16_overflow 0
		.amdhsa_tg_split 0
		.amdhsa_exception_fp_ieee_invalid_op 0
		.amdhsa_exception_fp_denorm_src 0
		.amdhsa_exception_fp_ieee_div_zero 0
		.amdhsa_exception_fp_ieee_overflow 0
		.amdhsa_exception_fp_ieee_underflow 0
		.amdhsa_exception_fp_ieee_inexact 0
		.amdhsa_exception_int_div_zero 0
	.end_amdhsa_kernel

.LBB6_4:
	s_lshl_b32 s18, s20, 8
	s_and_b32 s18, s18, 0x300
	s_lshl_b64 s[0:1], s[0:1], 10
	s_or_b32 s0, s0, s18
	s_lshl_b32 s18, s33, 5
	s_add_u32 s18, s0, s18
	v_and_b32_e32 v203, 31, v0
	s_addc_u32 s19, s1, 0
	v_or_b32_e32 v2, s18, v203
	v_mov_b32_e32 v3, s19
	v_lshrrev_b32_e32 v204, 5, v1
	v_lshlrev_b64 v[4:5], 13, v[2:3]
	v_lshlrev_b64 v[2:3], 10, v[2:3]
	v_lshl_add_u64 v[4:5], s[14:15], 0, v[4:5]
	v_lshlrev_b32_e32 v26, 4, v204
	v_mov_b32_e32 v27, 0
	v_lshl_add_u64 v[2:3], s[8:9], 0, v[2:3]
	v_lshl_add_u64 v[24:25], v[4:5], 0, v[26:27]
	v_lshl_add_u64 v[2:3], v[2:3], 0, s[6:7]
	v_and_b32_e32 v26, 32, v0
	v_lshl_add_u64 v[30:31], v[2:3], 0, v[26:27]
	global_load_dwordx4 v[100:103], v[30:31], off offset:16
	global_load_dwordx4 v[96:99], v[30:31], off
	s_and_b64 vcc, exec, s[4:5]
	s_cbranch_vccnz .LBB6_6
	s_mov_b64 s[0:1], 0x20000
	s_cmp_lg_u32 0, -1
	v_lshl_add_u64 v[24:25], v[20:21], 0, s[0:1]
	s_cselect_b32 s0, 0, 0
	s_add_i32 s0, s0, s36
	s_addk_i32 s0, 0x4000
	s_mov_b32 m0, s0
	s_nop 0
	global_load_lds_dwordx4 v[24:25], off
.LBB6_6:
	v_lshlrev_b32_e32 v30, 3, v22
	v_or_b32_e32 v22, s18, v28
	v_mov_b32_e32 v23, s19
	v_lshlrev_b64 v[22:23], 13, v[22:23]
	v_lshl_add_u64 v[80:81], s[14:15], 0, v[22:23]
	v_lshrrev_b32_e32 v104, 2, v203
	v_lshlrev_b32_e32 v22, 1, v204
	v_bfe_u32 v23, v203, 2, 2
	s_lshl_b32 s7, s33, 13
	v_bitop3_b32 v24, v22, v104, 3 bitop3:0x78
	v_bitop3_b32 v22, v22, v23, 1 bitop3:0x36
	s_cmp_lg_u32 0, -1
	v_lshlrev_b32_e32 v218, 4, v22
	v_bitop3_b32 v22, v28, v0, 15 bitop3:0x78
	s_cselect_b32 s0, 0, 0
	v_lshlrev_b32_e32 v26, 4, v22
	s_add_i32 s41, s0, s7
	v_lshl_add_u64 v[164:165], v[80:81], 0, v[26:27]
	s_mov_b64 s[0:1], 0x0
	v_and_b32_e32 v31, 15, v0
	v_lshl_add_u64 v[22:23], v[164:165], 0, s[0:1]
	s_add_i32 s38, s41, 0x14800
	s_mov_b32 m0, s38
	s_nop 0
	global_load_lds_dwordx4 v[22:23], off nt
	v_bitop3_b32 v22, v28, v31, 4 bitop3:0x36
	v_lshlrev_b32_e32 v26, 4, v22
	v_lshl_add_u64 v[22:23], v[80:81], 0, v[26:27]
	s_mov_b64 s[8:9], 0x8000
	v_lshlrev_b32_e32 v217, 4, v24
	v_lshl_add_u64 v[24:25], v[22:23], 0, s[8:9]
	s_add_i32 s8, s41, 0x14c00
	s_mov_b32 m0, s8
	s_nop 0
	global_load_lds_dwordx4 v[24:25], off nt
	v_bitop3_b32 v24, v28, v31, 8 bitop3:0x36
	v_lshlrev_b32_e32 v26, 4, v24
	v_lshl_add_u64 v[24:25], v[80:81], 0, v[26:27]
	s_mov_b64 s[8:9], 0x10000
	v_bitop3_b32 v26, v28, v31, 12 bitop3:0x36
	v_lshl_add_u64 v[82:83], v[24:25], 0, s[8:9]
	s_add_i32 s8, s41, 0x15000
	s_mov_b32 m0, s8
	s_nop 0
	global_load_lds_dwordx4 v[82:83], off nt
	v_lshlrev_b32_e32 v26, 4, v26
	v_lshl_add_u64 v[26:27], v[80:81], 0, v[26:27]
	s_mov_b64 s[8:9], 0x18000
	v_lshl_add_u64 v[80:81], v[26:27], 0, s[8:9]
	s_add_i32 s8, s41, 0x15400
	s_mov_b32 m0, s8
	s_nop 0
	global_load_lds_dwordx4 v[80:81], off nt
	s_mov_b64 s[14:15], 0x20000
	v_lshl_add_u64 v[80:81], v[164:165], 0, s[14:15]
	s_add_i32 s14, s41, 0x15800
	s_mov_b32 m0, s14
	s_nop 0
	global_load_lds_dwordx4 v[80:81], off nt
	s_mov_b64 s[14:15], 0x28000
	v_lshl_add_u64 v[80:81], v[22:23], 0, s[14:15]
	s_add_i32 s14, s41, 0x15c00
	s_mov_b32 m0, s14
	s_nop 0
	global_load_lds_dwordx4 v[80:81], off nt
	s_mov_b64 s[34:35], 0x30000
	v_lshl_add_u64 v[80:81], v[24:25], 0, s[34:35]
	s_add_i32 s34, s41, 0x16000
	s_mov_b32 m0, s34
	s_nop 0
	global_load_lds_dwordx4 v[80:81], off nt
	s_mov_b64 s[34:35], 0x38000
	v_lshl_add_u32 v216, v203, 6, 0
	v_lshl_add_u64 v[80:81], v[26:27], 0, s[34:35]
	s_add_i32 s41, s41, 0x16400
	s_mov_b32 m0, s41
	s_nop 0
	global_load_lds_dwordx4 v[80:81], off nt
	s_waitcnt vmcnt(0) lgkmcnt(0)
	s_barrier
	v_and_b32_e32 v226, 31, v0
	v_bfe_u32 v227, v0, 5, 1
	v_lshrrev_b32_e32 v228, 2, v226
	v_lshlrev_b32_e32 v228, 10, v228
	v_and_b32_e32 v229, 3, v226
	v_lshlrev_b32_e32 v229, 8, v229
	v_add3_u32 v230, s38, v228, v229
	v_and_b32_e32 v231, 15, v226
	v_xor_b32_e32 v231, v231, v227
	v_lshlrev_b32_e32 v231, 4, v231
	v_mov_b32_e32 v232, v231
	v_add_u32_e32 v232, v230, v232
	ds_read_b128 v[64:67], v232
	v_xor_b32_e32 v233, 0x80, v231
	v_add_u32_e32 v233, v230, v233
	ds_read_b128 v[2:5], v233
	v_xor_b32_e32 v234, 0x20, v231
	v_add_u32_e32 v234, v230, v234
	ds_read_b128 v[68:71], v234
	v_xor_b32_e32 v235, 0xa0, v231
	v_add_u32_e32 v235, v230, v235
	ds_read_b128 v[6:9], v235
	v_xor_b32_e32 v236, 0x40, v231
	v_add_u32_e32 v236, v230, v236
	ds_read_b128 v[72:75], v236
	v_xor_b32_e32 v237, 0xc0, v231
	v_add_u32_e32 v237, v230, v237
	ds_read_b128 v[10:13], v237
	v_xor_b32_e32 v238, 0x60, v231
	v_add_u32_e32 v238, v230, v238
	ds_read_b128 v[76:79], v238
	v_xor_b32_e32 v239, 0xe0, v231
	v_add_u32_e32 v239, v230, v239
	ds_read_b128 v[14:17], v239
	s_waitcnt lgkmcnt(0)
	s_mov_b64 s[52:53], 0x100
	v_lshl_add_u64 v[224:225], v[164:165], 0, s[52:53]
	s_add_i32 s54, s38, 0x0
	s_mov_b32 m0, s54
	s_nop 0
	global_load_lds_dwordx4 v[224:225], off nt
	s_mov_b64 s[52:53], 0x8100
	v_lshl_add_u64 v[224:225], v[22:23], 0, s[52:53]
	s_add_i32 s54, s38, 0x400
	s_mov_b32 m0, s54
	s_nop 0
	global_load_lds_dwordx4 v[224:225], off nt
	s_mov_b64 s[52:53], 0x10100
	v_lshl_add_u64 v[224:225], v[24:25], 0, s[52:53]
	s_add_i32 s54, s38, 0x800
	s_mov_b32 m0, s54
	s_nop 0
	global_load_lds_dwordx4 v[224:225], off nt
	s_mov_b64 s[52:53], 0x18100
	v_lshl_add_u64 v[224:225], v[26:27], 0, s[52:53]
	s_add_i32 s54, s38, 0xc00
	s_mov_b32 m0, s54
	s_nop 0
	global_load_lds_dwordx4 v[224:225], off nt
	s_mov_b64 s[52:53], 0x20100
	v_lshl_add_u64 v[224:225], v[164:165], 0, s[52:53]
	s_add_i32 s54, s38, 0x1000
	s_mov_b32 m0, s54
	s_nop 0
	global_load_lds_dwordx4 v[224:225], off nt
	s_mov_b64 s[52:53], 0x28100
	v_lshl_add_u64 v[224:225], v[22:23], 0, s[52:53]
	s_add_i32 s54, s38, 0x1400
	s_mov_b32 m0, s54
	s_nop 0
	global_load_lds_dwordx4 v[224:225], off nt
	s_mov_b64 s[52:53], 0x30100
	v_lshl_add_u64 v[224:225], v[24:25], 0, s[52:53]
	s_add_i32 s54, s38, 0x1800
	s_mov_b32 m0, s54
	s_nop 0
	global_load_lds_dwordx4 v[224:225], off nt
	s_mov_b64 s[52:53], 0x38100
	v_lshl_add_u64 v[224:225], v[26:27], 0, s[52:53]
	s_add_i32 s54, s38, 0x1c00
	s_mov_b32 m0, s54
	s_nop 0
	global_load_lds_dwordx4 v[224:225], off nt
	v_add_u32_e32 v209, v216, v217
	v_add_u32_e32 v210, v216, v218
	ds_read_b128 v[80:83], v209
	ds_read_b128 v[88:91], v209 offset:2048
	ds_read_b128 v[84:87], v210
	ds_read_b128 v[92:95], v210 offset:2048
	v_mov_b32_e32 v219, 0x7f7f7f7f
	v_mov_b32_e32 v220, 0x7c7c7c7c
	s_waitcnt vmcnt(10) lgkmcnt(1)
	v_mfma_scale_f32_32x32x64_f8f6f4 v[64:79], v[80:87], v[96:103], v[64:79], v219, v220 op_sel_hi:[0,0,0]
	s_waitcnt vmcnt(8) lgkmcnt(0)
	v_mfma_scale_f32_32x32x64_f8f6f4 v[2:17], v[88:95], v[96:103], v[2:17], v219, v220 op_sel_hi:[0,0,0]
	s_mov_b32 s41, 0x3fb8aa3b
	s_nop 15
	s_nop 15
	s_nop 15
	s_nop 15
	s_nop 15
	s_nop 15
	s_waitcnt vmcnt(0) lgkmcnt(0)
	s_barrier
	v_lshlrev_b32_e32 v29, 2, v204
	v_max_f32_e32 v80, v65, v65
	v_max_f32_e32 v81, v64, v64
	v_max_f32_e32 v80, v81, v80
	v_max3_f32 v81, v66, v67, v3
	v_max3_f32 v80, v80, v2, v4
	v_max3_f32 v80, v80, v5, v68
	v_max3_f32 v81, v81, v70, v71
	v_max3_f32 v80, v80, v69, v6
	v_max3_f32 v81, v81, v8, v9
	v_max3_f32 v80, v80, v7, v72
	v_max3_f32 v81, v81, v74, v75
	v_max3_f32 v80, v80, v73, v10
	v_max3_f32 v81, v81, v12, v13
	v_max3_f32 v80, v80, v11, v76
	v_max3_f32 v81, v81, v78, v79
	v_max3_f32 v80, v80, v77, v14
	v_max3_f32 v81, v81, v16, v17
	v_max3_f32 v80, v80, v15, v81
	v_mov_b32_e32 v81, v80
	s_nop 1
	v_permlane32_swap_b32_e32 v80, v81
	v_max_f32_e32 v81, v81, v81
	v_max_f32_e32 v80, v80, v80
	v_max_f32_e32 v80, v80, v81
	v_mul_f32_e32 v208, 0x3fb8aa3b, v80
	s_mov_b32 s27, 0
	s_mov_b32 s40, -1
	s_mov_b64 s[0:1], 0x8000
	s_mov_b64 s[28:29], 0x10000
	s_mov_b64 s[20:21], 0x18000
	s_mov_b64 s[8:9], 0x20000
	s_mov_b64 s[30:31], 0x28000
	s_mov_b64 s[14:15], 0x30000
	s_mov_b64 s[34:35], 0x38000
	v_fma_f32 v64, v64, s41, -v208
	v_fma_f32 v2, v2, s41, -v208
	v_fma_f32 v65, v65, s41, -v208
	v_fma_f32 v3, v3, s41, -v208
	v_fma_f32 v66, v66, s41, -v208
	v_fma_f32 v4, v4, s41, -v208
	v_fma_f32 v67, v67, s41, -v208
	v_fma_f32 v5, v5, s41, -v208
	v_fma_f32 v68, v68, s41, -v208
	v_fma_f32 v6, v6, s41, -v208
	v_fma_f32 v69, v69, s41, -v208
	v_fma_f32 v7, v7, s41, -v208
	v_fma_f32 v70, v70, s41, -v208
	v_fma_f32 v8, v8, s41, -v208
	v_fma_f32 v71, v71, s41, -v208
	v_fma_f32 v9, v9, s41, -v208
	v_fma_f32 v72, v72, s41, -v208
	v_fma_f32 v10, v10, s41, -v208
	v_fma_f32 v73, v73, s41, -v208
	v_fma_f32 v11, v11, s41, -v208
	v_fma_f32 v74, v74, s41, -v208
	v_fma_f32 v12, v12, s41, -v208
	v_fma_f32 v75, v75, s41, -v208
	v_fma_f32 v13, v13, s41, -v208
	v_fma_f32 v76, v76, s41, -v208
	v_fma_f32 v14, v14, s41, -v208
	v_fma_f32 v77, v77, s41, -v208
	v_fma_f32 v78, v78, s41, -v208
	v_fma_f32 v79, v79, s41, -v208
	v_fma_f32 v94, v15, s41, -v208
	v_fma_f32 v16, v16, s41, -v208
	v_fma_f32 v15, v17, s41, -v208
	s_and_b64 vcc, exec, s[4:5]
	s_cbranch_vccnz .LBB6_8
	v_lshl_add_u64 v[20:21], v[20:21], 0, s[14:15]
	s_mov_b32 m0, s39
	s_nop 0
	global_load_lds_dwordx4 v[20:21], off

	.amdhsa_kernel _Z6k_attnILi1024ELi2048ELi1024ELi1024ELi2048ELi1024ELb1ELb1EEvPKDF16_S1_S1_PKfPDF16_
		.amdhsa_group_segment_fixed_size 0
		.amdhsa_private_segment_fixed_size 0
		.amdhsa_kernarg_size 40
		.amdhsa_user_sgpr_count 2
		.amdhsa_user_sgpr_dispatch_ptr 0
		.amdhsa_user_sgpr_queue_ptr 0
		.amdhsa_user_sgpr_kernarg_segment_ptr 1
		.amdhsa_user_sgpr_dispatch_id 0
		.amdhsa_user_sgpr_kernarg_preload_length 0
		.amdhsa_user_sgpr_kernarg_preload_offset 0
		.amdhsa_user_sgpr_private_segment_size 0
		.amdhsa_uses_dynamic_stack 0
		.amdhsa_enable_private_segment 0
		.amdhsa_system_sgpr_workgroup_id_x 1
		.amdhsa_system_sgpr_workgroup_id_y 0
		.amdhsa_system_sgpr_workgroup_id_z 0
		.amdhsa_system_sgpr_workgroup_info 0
		.amdhsa_system_vgpr_workitem_id 0
		.amdhsa_next_free_vgpr 240
		.amdhsa_next_free_sgpr 56
		.amdhsa_accum_offset 240
		.amdhsa_reserve_vcc 1
		.amdhsa_float_round_mode_32 0
		.amdhsa_float_round_mode_16_64 0
		.amdhsa_float_denorm_mode_32 3
		.amdhsa_float_denorm_mode_16_64 3
		.amdhsa_dx10_clamp 1
		.amdhsa_ieee_mode 1
		.amdhsa_fp16_overflow 0
		.amdhsa_tg_split 0
		.amdhsa_exception_fp_ieee_invalid_op 0
		.amdhsa_exception_fp_denorm_src 0
		.amdhsa_exception_fp_ieee_div_zero 0
		.amdhsa_exception_fp_ieee_overflow 0
		.amdhsa_exception_fp_ieee_underflow 0
		.amdhsa_exception_fp_ieee_inexact 0
		.amdhsa_exception_int_div_zero 0
	.end_amdhsa_kernel

amdhsa.kernels:
  - .agpr_count:     0
    .args:
      - .offset:         0
        .size:           384
        .value_kind:     by_value
    .group_segment_fixed_size: 5120
    .kernarg_segment_align: 8
    .kernarg_segment_size: 384
    .language:       OpenCL C
    .language_version:
      - 2
      - 0
    .max_flat_workgroup_size: 256
    .name:           _Z6k_prep6WtArgs
    .private_segment_fixed_size: 0
    .sgpr_count:     38
    .sgpr_spill_count: 0
    .symbol:         _Z6k_prep6WtArgs.kd
    .uniform_work_group_size: 1
    .uses_dynamic_stack: false
    .vgpr_count:     29
    .vgpr_spill_count: 0
    .wavefront_size: 64
  - .agpr_count:     0
    .args:
      - .actual_access:  read_only
        .address_space:  global
        .offset:         0
        .size:           8
        .value_kind:     global_buffer
      - .actual_access:  read_only
        .address_space:  global
        .offset:         8
        .size:           8
        .value_kind:     global_buffer
      - .actual_access:  read_only
        .address_space:  global
        .offset:         16
        .size:           8
        .value_kind:     global_buffer
      - .actual_access:  write_only
        .address_space:  global
        .offset:         24
        .size:           8
        .value_kind:     global_buffer
      - .actual_access:  write_only
        .address_space:  global
        .offset:         32
        .size:           8
        .value_kind:     global_buffer
      - .actual_access:  write_only
        .address_space:  global
        .offset:         40
        .size:           8
        .value_kind:     global_buffer
      - .offset:         48
        .size:           4
        .value_kind:     by_value
    .group_segment_fixed_size: 0
    .kernarg_segment_align: 8
    .kernarg_segment_size: 52
    .language:       OpenCL C
    .language_version:
      - 2
      - 0
    .max_flat_workgroup_size: 256
    .name:           _Z4k_lnPKDF16_PKfS2_PfPDF16_Phi
    .private_segment_fixed_size: 0
    .sgpr_count:     18
    .sgpr_spill_count: 0
    .symbol:         _Z4k_lnPKDF16_PKfS2_PfPDF16_Phi.kd
    .uniform_work_group_size: 1
    .uses_dynamic_stack: false
    .vgpr_count:     59
    .vgpr_spill_count: 0
    .wavefront_size: 64
  - .agpr_count:     0
    .args:
      - .offset:         0
        .size:           56
        .value_kind:     by_value
      - .offset:         56
        .size:           72
        .value_kind:     by_value
      - .offset:         128
        .size:           176
        .value_kind:     by_value
      - .address_space:  global
        .offset:         304
        .size:           8
        .value_kind:     global_buffer
      - .offset:         312
        .size:           4
        .value_kind:     hidden_block_count_x
      - .offset:         316
        .size:           4
        .value_kind:     hidden_block_count_y
      - .offset:         320
        .size:           4
        .value_kind:     hidden_block_count_z
      - .offset:         324
        .size:           2
        .value_kind:     hidden_group_size_x
      - .offset:         326
        .size:           2
        .value_kind:     hidden_group_size_y
      - .offset:         328
        .size:           2
        .value_kind:     hidden_group_size_z
      - .offset:         330
        .size:           2
        .value_kind:     hidden_remainder_x
      - .offset:         332
        .size:           2
        .value_kind:     hidden_remainder_y
      - .offset:         334
        .size:           2
        .value_kind:     hidden_remainder_z
      - .offset:         352
        .size:           8
        .value_kind:     hidden_global_offset_x
      - .offset:         360
        .size:           8
        .value_kind:     hidden_global_offset_y
      - .offset:         368
        .size:           8
        .value_kind:     hidden_global_offset_z
      - .offset:         376
        .size:           2
        .value_kind:     hidden_grid_dims
      - .offset:         432
        .size:           4
        .value_kind:     hidden_dynamic_lds_size
    .group_segment_fixed_size: 0
    .kernarg_segment_align: 8
    .kernarg_segment_size: 568
    .language:       OpenCL C
    .language_version:
      - 2
      - 0
    .max_flat_workgroup_size: 512
    .name:           _Z6k_gemmIN3pg84EpiHILi0ELb1EEELb1EEvNS0_4GemmET_6WtTailPj
    .private_segment_fixed_size: 0
    .sgpr_count:     62
    .sgpr_spill_count: 5
    .symbol:         _Z6k_gemmIN3pg84EpiHILi0ELb1EEELb1EEvNS0_4GemmET_6WtTailPj.kd
    .uniform_work_group_size: 1
    .uses_dynamic_stack: false
    .vgpr_count:     240
    .vgpr_spill_count: 0
    .wavefront_size: 64
  - .agpr_count:     0
    .args:
      - .address_space:  global
        .offset:         0
        .size:           8
        .value_kind:     global_buffer
      - .address_space:  global
        .offset:         8
        .size:           8
        .value_kind:     global_buffer
      - .address_space:  global
        .offset:         16
        .size:           8
        .value_kind:     global_buffer
      - .address_space:  global
        .offset:         24
        .size:           8
        .value_kind:     global_buffer
      - .address_space:  global
        .offset:         32
        .size:           8
        .value_kind:     global_buffer
    .group_segment_fixed_size: 0
    .kernarg_segment_align: 8
    .kernarg_segment_size: 40
    .language:       OpenCL C
    .language_version:
      - 2
      - 0
    .max_flat_workgroup_size: 512
    .name:           _Z6k_attnILi1024ELi1024ELi1024ELi1024ELi3072ELi1024ELb1ELb1EEvPKDF16_S1_S1_PKfPDF16_
    .private_segment_fixed_size: 0
    .sgpr_count:     55
    .sgpr_spill_count: 0
    .symbol:         _Z6k_attnILi1024ELi1024ELi1024ELi1024ELi3072ELi1024ELb1ELb1EEvPKDF16_S1_S1_PKfPDF16_.kd
    .uniform_work_group_size: 1
    .uses_dynamic_stack: false
    .vgpr_count:     224
    .vgpr_spill_count: 0
    .wavefront_size: 64
  - .agpr_count:     0
    .args:
      - .address_space:  global
        .offset:         0
        .size:           8
        .value_kind:     global_buffer
      - .address_space:  global
        .offset:         8
        .size:           8
        .value_kind:     global_buffer
      - .offset:         16
        .size:           4
        .value_kind:     by_value
      - .offset:         20
        .size:           4
        .value_kind:     by_value
      - .offset:         24
        .size:           4
        .value_kind:     by_value
      - .offset:         32
        .size:           32
        .value_kind:     by_value
    .group_segment_fixed_size: 0
    .kernarg_segment_align: 8
    .kernarg_segment_size: 64
    .language:       OpenCL C
    .language_version:
      - 2
      - 0
    .max_flat_workgroup_size: 512
    .name:           _ZN2g811k_gemm128f8INS_6EpiResEEEvPKhS3_iiiT_
    .private_segment_fixed_size: 0
    .sgpr_count:     34
    .sgpr_spill_count: 0
    .symbol:         _ZN2g811k_gemm128f8INS_6EpiResEEEvPKhS3_iiiT_.kd
    .uniform_work_group_size: 1
    .uses_dynamic_stack: false
    .vgpr_count:     98
    .vgpr_spill_count: 0
    .wavefront_size: 64
  - .agpr_count:     0
    .args:
      - .address_space:  global
        .offset:         0
        .size:           8
        .value_kind:     global_buffer
      - .address_space:  global
        .offset:         8
        .size:           8
        .value_kind:     global_buffer
      - .offset:         16
        .size:           4
        .value_kind:     by_value
      - .offset:         20
        .size:           4
        .value_kind:     by_value
      - .offset:         24
        .size:           4
        .value_kind:     by_value
      - .offset:         32
        .size:           16
        .value_kind:     by_value
    .group_segment_fixed_size: 0
    .kernarg_segment_align: 8
    .kernarg_segment_size: 48
    .language:       OpenCL C
    .language_version:
      - 2
      - 0
    .max_flat_workgroup_size: 512
    .name:           _ZN2g811k_gemm128f8INS_5EpiQ8EEEvPKhS3_iiiT_
    .private_segment_fixed_size: 0
    .sgpr_count:     62
    .sgpr_spill_count: 0
    .symbol:         _ZN2g811k_gemm128f8INS_5EpiQ8EEEvPKhS3_iiiT_.kd
    .uniform_work_group_size: 1
    .uses_dynamic_stack: false
    .vgpr_count:     240
    .vgpr_spill_count: 0
    .wavefront_size: 64
  - .agpr_count:     0
    .args:
      - .address_space:  global
        .offset:         0
        .size:           8
        .value_kind:     global_buffer
      - .address_space:  global
        .offset:         8
        .size:           8
        .value_kind:     global_buffer
      - .address_space:  global
        .offset:         16
        .size:           8
        .value_kind:     global_buffer
      - .address_space:  global
        .offset:         24
        .size:           8
        .value_kind:     global_buffer
      - .address_space:  global
        .offset:         32
        .size:           8
        .value_kind:     global_buffer
    .group_segment_fixed_size: 0
    .kernarg_segment_align: 8
    .kernarg_segment_size: 40
    .language:       OpenCL C
    .language_version:
      - 2
      - 0
    .max_flat_workgroup_size: 512
    .name:           _Z6k_attnILi1024ELi2048ELi1024ELi1024ELi2048ELi1024ELb1ELb1EEvPKDF16_S1_S1_PKfPDF16_
    .private_segment_fixed_size: 0
    .sgpr_count:     52
    .sgpr_spill_count: 0
    .symbol:         _Z6k_attnILi1024ELi2048ELi1024ELi1024ELi2048ELi1024ELb1ELb1EEvPKDF16_S1_S1_PKfPDF16_.kd
    .uniform_work_group_size: 1
    .uses_dynamic_stack: false
    .vgpr_count:     224
    .vgpr_spill_count: 0
    .wavefront_size: 64
  - .agpr_count:     0
    .args:
      - .offset:         0
        .size:           56
        .value_kind:     by_value
      - .offset:         56
        .size:           72
        .value_kind:     by_value
      - .offset:         128
        .size:           176
        .value_kind:     by_value
      - .address_space:  global
        .offset:         304
        .size:           8
        .value_kind:     global_buffer
      - .offset:         312
        .size:           4
        .value_kind:     hidden_block_count_x
      - .offset:         316
        .size:           4
        .value_kind:     hidden_block_count_y
      - .offset:         320
        .size:           4
        .value_kind:     hidden_block_count_z
      - .offset:         324
        .size:           2
        .value_kind:     hidden_group_size_x
      - .offset:         326
        .size:           2
        .value_kind:     hidden_group_size_y
      - .offset:         328
        .size:           2
        .value_kind:     hidden_group_size_z
      - .offset:         330
        .size:           2
        .value_kind:     hidden_remainder_x
      - .offset:         332
        .size:           2
        .value_kind:     hidden_remainder_y
      - .offset:         334
        .size:           2
        .value_kind:     hidden_remainder_z
      - .offset:         352
        .size:           8
        .value_kind:     hidden_global_offset_x
      - .offset:         360
        .size:           8
        .value_kind:     hidden_global_offset_y
      - .offset:         368
        .size:           8
        .value_kind:     hidden_global_offset_z
      - .offset:         376
        .size:           2
        .value_kind:     hidden_grid_dims
      - .offset:         432
        .size:           4
        .value_kind:     hidden_dynamic_lds_size
    .group_segment_fixed_size: 0
    .kernarg_segment_align: 8
    .kernarg_segment_size: 568
    .language:       OpenCL C
    .language_version:
      - 2
      - 0
    .max_flat_workgroup_size: 512
    .name:           _Z6k_gemmIN3pg84EpiHILi1ELb0EEELb0EEvNS0_4GemmET_6WtTailPj
    .private_segment_fixed_size: 0
    .sgpr_count:     85
    .sgpr_spill_count: 0
    .symbol:         _Z6k_gemmIN3pg84EpiHILi1ELb0EEELb0EEvNS0_4GemmET_6WtTailPj.kd
    .uniform_work_group_size: 1
    .uses_dynamic_stack: false
    .vgpr_count:     242
    .vgpr_spill_count: 0
    .wavefront_size: 64
  - .agpr_count:     0
    .args:
      - .address_space:  global
        .offset:         0
        .size:           8
        .value_kind:     global_buffer
      - .address_space:  global
        .offset:         8
        .size:           8
        .value_kind:     global_buffer
      - .offset:         16
        .size:           4
        .value_kind:     by_value
      - .offset:         20
        .size:           4
        .value_kind:     by_value
      - .offset:         24
        .size:           4
        .value_kind:     by_value
      - .offset:         32
        .size:           32
        .value_kind:     by_value
    .group_segment_fixed_size: 0
    .kernarg_segment_align: 8
    .kernarg_segment_size: 64
    .language:       OpenCL C
    .language_version:
      - 2
      - 0
    .max_flat_workgroup_size: 512
    .name:           _ZN4g1289k_gemm128INS_8EpiRes16EEEvPKDF16_S3_iiiT_
    .private_segment_fixed_size: 0
    .sgpr_count:     35
    .sgpr_spill_count: 0
    .symbol:         _ZN4g1289k_gemm128INS_8EpiRes16EEEvPKDF16_S3_iiiT_.kd
    .uniform_work_group_size: 1
    .uses_dynamic_stack: false
    .vgpr_count:     112
    .vgpr_spill_count: 0
    .wavefront_size: 64
